# v030 with the second conversion item issued right after the first barrier instead of after the second (prefetch distance tuning)
# baseline (speedup 1.0000x reference)
.LBB0_424:
	s_bitcmp1_b32 s7, 0
	s_cselect_b32 s28, 0x520, 0
	s_waitcnt lgkmcnt(0)
	s_barrier
	s_sub_u32 s98, s7, 2
	s_cmp_lt_u32 s98, 53
	s_cbranch_scc0 .Lcv2m_skip
	s_bitcmp1_b32 s7, 0
	s_cbranch_scc1 .Lcv2m_skip
	v_readlane_b32 s100, v255, 48
	v_readlane_b32 s101, v255, 49
	s_add_u32 s100, s100, 0x1000000
	s_addc_u32 s101, s101, 0
	v_writelane_b32 v255, s100, 48
	v_writelane_b32 v255, s101, 49
	global_load_dwordx4 v[2:5], v250, s[100:101]
	v_add_u32_e32 v253, 0x2000, v250
	global_load_dwordx4 v[6:9], v253, s[100:101]
	v_add_u32_e32 v252, 0x4000, v250
	global_load_dwordx4 v[10:13], v252, s[100:101]
	v_add_u32_e32 v253, 0x6000, v250
	global_load_dwordx4 v[14:17], v253, s[100:101]
	v_add_u32_e32 v252, 0x8000, v250
	global_load_dwordx4 v[18:21], v252, s[100:101]
	v_add_u32_e32 v253, 0xa000, v250
	global_load_dwordx4 v[22:25], v253, s[100:101]
	v_add_u32_e32 v252, 0xc000, v250
	global_load_dwordx4 v[26:29], v252, s[100:101]
	v_add_u32_e32 v253, 0xe000, v250
	global_load_dwordx4 v[116:119], v253, s[100:101]
.Lcv2m_skip:
	s_add_i32 s60, s28, 0
	s_add_i32 s60, s60, 0x1e040
	s_and_saveexec_b64 s[28:29], s[4:5]
	s_cbranch_execz .LBB0_427
	v_lshl_add_u32 v98, v125, 2, s60
	ds_read_b32 v98, v98 offset:1024
	v_lshlrev_b32_e32 v99, 16, v94
	v_and_b32_e32 v94, 0xffff0000, v94
	v_readlane_b32 s30, v255, 34
	v_readlane_b32 s31, v255, 35
	s_waitcnt lgkmcnt(0)
	v_mul_f32_e32 v99, v98, v99
	v_mul_f32_e32 v94, v98, v94
	v_cvt_pk_bf16_f32 v94, v99, v94
	v_lshlrev_b32_e32 v99, 16, v95
	v_and_b32_e32 v95, 0xffff0000, v95
	v_mul_f32_e32 v99, v98, v99
	v_mul_f32_e32 v95, v98, v95
	v_cvt_pk_bf16_f32 v95, v99, v95
	v_lshlrev_b32_e32 v99, 16, v96
	v_and_b32_e32 v96, 0xffff0000, v96
	v_mul_f32_e32 v99, v98, v99
	v_mul_f32_e32 v96, v98, v96
	v_cvt_pk_bf16_f32 v96, v99, v96
	v_lshlrev_b32_e32 v99, 16, v97
	v_and_b32_e32 v97, 0xffff0000, v97
	v_mul_f32_e32 v97, v98, v97
	v_mul_f32_e32 v99, v98, v99
	v_cvt_pk_bf16_f32 v97, v99, v97
	ds_write_b128 v143, v[94:97]
	s_and_b64 exec, exec, s[30:31]
	v_bfe_u32 v94, v98, 16, 1
	s_movk_i32 s30, 0x7fff
	v_add3_u32 v94, v98, v94, s30
	ds_write_b16_d16_hi v129, v94 offset:64
